# P11: row sum-of-squares partials requested inside the first K-iteration instead of behind a vmcnt(0) drain in the epilogue
# baseline (speedup 1.0000x reference)
.Lphr_0:
	ds_read_b128 v[18:21], v177
	ds_read_b128 v[22:25], v178
	ds_read_b128 v[26:29], v185
	ds_read_b128 v[30:33], v186
	ds_read_b128 v[2:5], v179
	ds_read_b128 v[6:9], v180
	ds_read_b128 v[10:13], v187
	ds_read_b128 v[14:17], v188
	s_add_i32 s75, s92, 0x80
	s_and_b64 s[30:31], s[30:31], exec
	s_cselect_b32 s75, s75, s91
	s_cselect_b32 s96, s93, s29
	s_add_i32 s30, s75, 0x80
	s_add_i32 s31, s96, 0x80
	v_mov_b32_e32 v162, v1
	ds_read_b128 v[198:201], v193
	ds_read_b128 v[202:205], v193 offset:1024
	ds_read_b128 v[214:217], v193 offset:2048
	ds_read_b128 v[218:221], v193 offset:3072
	ds_read_b128 v[222:225], v193 offset:4096
	ds_read_b128 v[226:229], v193 offset:5120
	ds_read_b128 v[230:233], v193 offset:6144
	ds_read_b128 v[234:237], v193 offset:7168
	s_add_i32 s97, s92, s65
	v_add_u32_e32 v162, s97, v162
	s_add_i32 m0, s47, 0xc000
	s_add_i32 s97, s92, s74
	global_load_lds_dwordx4 v162, s[10:11]
	v_mov_b32_e32 v162, v1
	s_add_i32 m0, s47, 0xe000
	v_add_u32_e32 v162, s97, v162
	global_load_lds_dwordx4 v162, s[10:11]
	s_waitcnt vmcnt(8)
	s_waitcnt lgkmcnt(0)
	s_barrier
	s_setprio 1
	s_waitcnt lgkmcnt(0)
	v_mfma_f32_16x16x128_f8f6f4 v[158:161], v[18:25], v[198:205], 0
	v_mfma_f32_16x16x128_f8f6f4 v[150:153], v[26:33], v[198:205], 0
	v_mfma_f32_16x16x128_f8f6f4 v[142:145], v[18:25], v[214:221], 0
	v_mfma_f32_16x16x128_f8f6f4 v[134:137], v[26:33], v[214:221], 0
	v_mfma_f32_16x16x128_f8f6f4 v[126:129], v[18:25], v[222:229], 0
	v_mfma_f32_16x16x128_f8f6f4 v[118:121], v[26:33], v[222:229], 0
	v_mfma_f32_16x16x128_f8f6f4 v[110:113], v[18:25], v[230:237], 0
	v_mfma_f32_16x16x128_f8f6f4 v[102:105], v[26:33], v[230:237], 0
	s_setprio 0
	s_setprio 1
	v_mfma_f32_16x16x128_f8f6f4 v[154:157], v[2:9], v[198:205], 0
	v_mfma_f32_16x16x128_f8f6f4 v[146:149], v[10:17], v[198:205], 0
	v_mfma_f32_16x16x128_f8f6f4 v[138:141], v[2:9], v[214:221], 0
	v_mfma_f32_16x16x128_f8f6f4 v[130:133], v[10:17], v[214:221], 0
	v_mfma_f32_16x16x128_f8f6f4 v[122:125], v[2:9], v[222:229], 0
	v_mfma_f32_16x16x128_f8f6f4 v[114:117], v[10:17], v[222:229], 0
	v_mfma_f32_16x16x128_f8f6f4 v[106:109], v[2:9], v[230:237], 0
	v_mfma_f32_16x16x128_f8f6f4 v[98:101], v[10:17], v[230:237], 0
	s_setprio 0
	s_barrier
	v_mov_b32_e32 v162, v174
	ds_read_b128 v[198:201], v193 offset:16384
	ds_read_b128 v[202:205], v193 offset:17408
	ds_read_b128 v[214:217], v193 offset:18432
	ds_read_b128 v[218:221], v193 offset:19456
	ds_read_b128 v[222:225], v193 offset:20480
	ds_read_b128 v[226:229], v193 offset:21504
	ds_read_b128 v[230:233], v193 offset:22528
	ds_read_b128 v[234:237], v193 offset:23552
	s_mov_b32 m0, s48
	v_add_u32_e32 v162, s96, v162
	global_load_lds_dwordx4 v162, s[20:21]
	v_mov_b32_e32 v162, v174
	s_add_i32 s96, s96, s46
	v_add_u32_e32 v162, s96, v162
	s_mov_b32 m0, s49
	s_add_i32 s96, s96, s46
	global_load_lds_dwordx4 v162, s[20:21]
	v_mov_b32_e32 v162, v174
	s_mov_b32 m0, s50
	v_add_u32_e32 v162, s96, v162
	global_load_lds_dwordx4 v162, s[20:21]
	v_mov_b32_e32 v162, v174
	s_add_i32 s96, s96, s46
	v_add_u32_e32 v162, s96, v162
	s_mov_b32 m0, s51
	s_nop 0
	global_load_lds_dwordx4 v162, s[20:21]
	v_mov_b32_e32 v162, v1
	s_mov_b32 m0, s47
	v_add_u32_e32 v162, s75, v162
	global_load_lds_dwordx4 v162, s[10:11]
	v_mov_b32_e32 v162, v1
	s_add_i32 s75, s75, s45
	v_add_u32_e32 v162, s75, v162
	s_mov_b32 m0, s52
	s_nop 0
	global_load_lds_dwordx4 v162, s[10:11]
	s_waitcnt vmcnt(8)
	s_waitcnt lgkmcnt(0)
	s_barrier
	s_setprio 1
	s_waitcnt lgkmcnt(0)
	v_mfma_f32_16x16x128_f8f6f4 v[94:97], v[18:25], v[198:205], 0
	v_mfma_f32_16x16x128_f8f6f4 v[86:89], v[26:33], v[198:205], 0
	v_mfma_f32_16x16x128_f8f6f4 v[78:81], v[18:25], v[214:221], 0
	v_mfma_f32_16x16x128_f8f6f4 v[70:73], v[26:33], v[214:221], 0
	v_mfma_f32_16x16x128_f8f6f4 v[62:65], v[18:25], v[222:229], 0
	v_mfma_f32_16x16x128_f8f6f4 v[54:57], v[26:33], v[222:229], 0
	v_mfma_f32_16x16x128_f8f6f4 v[46:49], v[18:25], v[230:237], 0
	v_mfma_f32_16x16x128_f8f6f4 v[38:41], v[26:33], v[230:237], 0
	s_setprio 0
	s_setprio 1
	v_mfma_f32_16x16x128_f8f6f4 v[90:93], v[2:9], v[198:205], 0
	v_mfma_f32_16x16x128_f8f6f4 v[82:85], v[10:17], v[198:205], 0
	v_mfma_f32_16x16x128_f8f6f4 v[74:77], v[2:9], v[214:221], 0
	v_mfma_f32_16x16x128_f8f6f4 v[66:69], v[10:17], v[214:221], 0
	v_mfma_f32_16x16x128_f8f6f4 v[58:61], v[2:9], v[222:229], 0
	v_mfma_f32_16x16x128_f8f6f4 v[50:53], v[10:17], v[222:229], 0
	v_mfma_f32_16x16x128_f8f6f4 v[42:45], v[2:9], v[230:237], 0
	v_mfma_f32_16x16x128_f8f6f4 v[34:37], v[10:17], v[230:237], 0
	s_setprio 0
	s_barrier
	v_lshlrev_b32_e32 v211, 4, v176
	v_add3_u32 v211, s69, v175, v211
	v_and_b32_e32 v197, 1, v175
	v_ashrrev_i32_e32 v211, 1, v211
	v_lshlrev_b32_e32 v211, 7, v211
	v_lshl_add_u32 v211, v197, 6, v211
	s_lshl_b32 s100, s8, 15
	s_add_u32 s100, s56, s100
	s_addc_u32 s101, s57, 0
	global_load_dwordx4 v[238:241], v211, s[100:101]
	global_load_dwordx4 v[242:245], v211, s[100:101] offset:16
	global_load_dwordx4 v[246:249], v211, s[100:101] offset:32
	global_load_dwordx4 v[250:253], v211, s[100:101] offset:48
	s_branch .Lmidr_0

.LBB0_1402:
	v_mov_b32_e32 v20, v175
	v_mov_b32_e32 v26, v176
	s_lshl_b32 s4, s9, 10
	s_nop 15
	s_nop 15
	s_add_i32 s4, s72, s4
	s_cmp_lg_u32 s8, s28
	v_lshl_add_u32 v10, v26, 5, s4
	ds_read_b128 v[6:9], v10
	ds_read_b128 v[2:5], v10 offset:16
	ds_read_b128 v[14:17], v10 offset:512
	ds_read_b128 v[10:13], v10 offset:528
	s_mov_b64 s[4:5], -1
	s_cbranch_scc0 .LBB0_1406
	v_lshlrev_b32_e32 v18, 4, v26
	v_add3_u32 v18, s69, v20, v18
	s_ashr_i32 s9, s8, 31
	v_ashrrev_i32_e32 v18, 1, v18
	v_and_b32_e32 v27, 1, v20
	v_and_b32_e32 v21, 64, v195
	v_xor_b32_e32 v19, 1, v195
	v_add_u32_e32 v21, 64, v21
	v_cmp_lt_i32_e32 vcc, v19, v21
	s_nop 1
	v_cndmask_b32_e32 v21, v195, v19, vcc
	v_lshlrev_b32_e32 v21, 2, v21
	v_cmp_eq_u32_e32 vcc, 0, v27
	v_add_f32_e32 v19, v238, v239
	v_add_f32_e32 v22, v240, v241
	v_add_f32_e32 v23, v242, v243
	v_add_f32_e32 v24, v244, v245
	v_add_f32_e32 v25, v246, v247
	v_add_f32_e32 v28, v248, v249
	v_add_f32_e32 v29, v250, v251
	v_add_f32_e32 v30, v252, v253
	v_add_f32_e32 v19, v19, v22
	v_add_f32_e32 v22, v23, v24
	v_add_f32_e32 v23, v25, v28
	v_add_f32_e32 v24, v29, v30
	v_add_f32_e32 v19, v19, v22
	v_add_f32_e32 v22, v23, v24
	v_add_f32_e32 v19, v19, v22
	ds_bpermute_b32 v21, v21, v19
	s_and_saveexec_b64 s[4:5], vcc
	s_cbranch_execz .LBB0_1405
	s_waitcnt lgkmcnt(0)
	v_add_f32_e32 v19, v19, v21
	v_fmamk_f32 v19, v19, 0x3a000000, v194
	v_mul_f32_e32 v21, 0x4b800000, v19
	v_cmp_gt_f32_e32 vcc, s77, v19
	v_lshl_add_u32 v18, v18, 2, 0
	v_add_u32_e32 v18, 0x21000, v18
	v_cndmask_b32_e32 v19, v19, v21, vcc
	v_rsq_f32_e32 v19, v19
	s_nop 0
	v_mul_f32_e32 v21, 0x45800000, v19
	v_cndmask_b32_e32 v19, v19, v21, vcc
	ds_write_b32 v18, v19
